# weight-transpose work queue: next chunk index requested at chunk start instead of a serial atomic round trip between chunks
# speedup vs baseline: 1.0008x; 1.0008x over previous
.LBB0_30:
	s_barrier
	s_barrier
	s_load_dwordx2 s[8:9], s[28:29], 0xe0
	v_ashrrev_i32_e32 v7, 6, v6
	s_movk_i32 s0, 0x4100
	v_mul_lo_u32 v2, v7, s0
	v_writelane_b32 v254, s2, 7
	s_waitcnt lgkmcnt(0)
	s_add_u32 s6, s8, 0x8000
	s_addc_u32 s7, s9, 0
	s_add_u32 s0, s8, 0x1e10000
	s_addc_u32 s1, s9, 0
	s_add_u32 s2, s8, 0x23810000
	s_addc_u32 s3, s9, 0
	s_add_u32 s16, s8, 0x3810000
	s_addc_u32 s17, s9, 0
	s_add_u32 s18, s8, 0x3010000
	v_add_u32_e32 v5, 0, v2
	v_bfe_u32 v9, v6, 4, 2
	v_and_b32_e32 v2, 60, v1
	s_addc_u32 s19, s9, 0
	v_lshlrev_b32_e32 v1, 2, v9
	v_mul_u32_u24_e32 v4, 0x104, v2
	s_add_u32 s22, s8, 0x2810000
	v_add3_u32 v12, v5, v1, v4
	v_lshlrev_b32_e32 v1, 3, v6
	s_addc_u32 s23, s9, 0
	s_movk_i32 s4, 0x104
	v_bfe_u32 v13, v6, 3, 3
	v_and_b32_e32 v4, 56, v1
	v_mov_b32_e32 v11, 0x820
	s_add_u32 s24, s8, 0x73630000
	v_lshl_add_u32 v10, v4, 2, v5
	v_mad_u32_u24 v11, v13, s4, v11
	s_addc_u32 s25, s9, 0
	v_and_b32_e32 v8, 63, v6
	v_mov_b32_e32 v3, 0
	s_add_u32 s26, s8, 0x10000
	v_add_u32_e32 v26, v10, v11
	v_mov_b32_e32 v5, v3
	v_mad_u32_u24 v14, v13, s4, v10
	v_or_b32_e32 v15, 8, v13
	v_or_b32_e32 v16, 16, v13
	v_or_b32_e32 v17, 24, v13
	v_or_b32_e32 v18, 32, v13
	v_or_b32_e32 v19, 40, v13
	v_or_b32_e32 v20, 48, v13
	v_or_b32_e32 v21, 56, v13
	v_or_b32_e32 v22, 64, v13
	v_or_b32_e32 v23, 0x50, v13
	v_or_b32_e32 v24, 0x60, v13
	v_or_b32_e32 v25, 0x70, v13
	s_addc_u32 s27, s9, 0
	s_movk_i32 s30, 0x4000
	s_mov_b32 s31, 0x8000
	s_mov_b32 s33, 0xc000
	s_mov_b32 s34, 0x10000
	s_mov_b32 s35, 0x14000
	s_mov_b32 s36, 0x18000
	s_mov_b32 s37, 0x1c000
	s_mov_b32 s38, 0x20000
	s_mov_b32 s39, 0x24000
	s_mov_b32 s41, 0x28000
	s_mov_b32 s43, 0x2c000
	s_mov_b32 s46, 0x30000
	s_mov_b32 s47, 0x34000
	s_mov_b32 s48, 0x38000
	s_mov_b32 s49, 0x3c000
	s_mov_b32 s50, 0xc3e00000
	v_add_u32_e32 v27, 0x820, v26
	v_add_u32_e32 v28, 0x828, v26
	v_add_u32_e32 v29, 0x830, v26
	v_add_u32_e32 v30, 0x838, v26
	v_add_u32_e32 v31, 0x1040, v26
	v_add_u32_e32 v32, 0x1048, v26
	v_add_u32_e32 v33, 0x1050, v26
	v_add_u32_e32 v34, 0x1058, v26
	v_add_u32_e32 v35, 0x1860, v26
	v_add_u32_e32 v36, 0x1868, v26
	v_add_u32_e32 v37, 0x1870, v26
	v_add_u32_e32 v38, 0x1878, v26
	v_add_u32_e32 v39, 0x2080, v26
	v_add_u32_e32 v40, 0x2088, v26
	v_add_u32_e32 v41, 0x2090, v26
	v_add_u32_e32 v42, 0x2098, v26
	v_add_u32_e32 v43, 0x28a0, v26
	v_add_u32_e32 v44, 0x28a8, v26
	v_add_u32_e32 v45, 0x28b0, v26
	v_add_u32_e32 v46, 0x28b8, v26
	v_add_u32_e32 v47, 0x30c0, v26
	v_add_u32_e32 v48, 0x30c8, v26
	v_add_u32_e32 v49, 0x30d0, v26
	v_add_u32_e32 v50, 0x30d8, v26
	s_mov_b32 s51, 0x60000
	s_mov_b32 s52, 0x107000
	s_mov_b32 s53, 0x11a000
	s_movk_i32 s54, 0x1000
	s_mov_b32 s55, 0x27000
	s_mov_b32 s56, 0x3a000
	s_mov_b32 s57, 0x4d000
	s_mov_b32 s58, 0x73000
	s_mov_b32 s59, 0x86000
	s_mov_b32 s60, 0x99000
	s_mov_b32 s61, 0xac000
	s_mov_b32 s62, 0xbf000
	s_mov_b32 s63, 0xd2000
	s_mov_b32 s64, 0xe5000
	s_mov_b32 s65, 0xf8000
	s_mov_b32 s66, 0x10b000
	s_mov_b32 s67, 0x11e000
	s_mov_b32 s68, 0x13000
	s_mov_b32 s69, 0x26000
	s_mov_b32 s70, 0x39000
	s_mov_b32 s71, 0x4c000
	v_lshlrev_b32_e32 v2, 2, v2
	v_mov_b32_e32 v51, 0x43e00000
	s_mov_b32 s72, 0x5f000
	s_mov_b32 s73, 0x72000
	s_mov_b32 s74, 0x85000
	s_mov_b32 s75, 0x98000
	s_mov_b32 s76, 0xab000
	s_mov_b32 s77, 0xbe000
	s_mov_b32 s78, 0xd1000
	s_mov_b32 s79, 0xe4000
	s_mov_b32 s80, 0xf7000
	s_mov_b32 s81, 0x10a000
	s_mov_b32 s82, 0x11d000
	s_mov_b32 s9, 0
	v_cmp_eq_u32_e64 s[4:5], 0, v8
	s_nop 3
	s_and_saveexec_b64 s[10:11], s[4:5]
	v_mov_b32_e32 v255, 4
	global_atomic_add v255, v3, v255, s[6:7] sc0
	s_or_b64 exec, exec, s[10:11]
	s_branch .LBB0_33

.LBB0_33:
	v_mov_b32_e32 v10, v3
	s_and_saveexec_b64 s[10:11], s[4:5]
	s_cbranch_execz .LBB0_37
	s_mov_b64 s[14:15], exec
	v_mbcnt_lo_u32_b32 v10, s14, 0
	v_mbcnt_hi_u32_b32 v10, s15, v10
	v_cmp_eq_u32_e32 vcc, 0, v10
	s_and_saveexec_b64 s[12:13], vcc
	s_cbranch_execz .LBB0_36
	s_bcnt1_i32_b64 s8, s[14:15]
	s_lshl_b32 s8, s8, 2
	v_mov_b32_e32 v11, s8
	s_waitcnt vmcnt(0)
	v_mov_b32_e32 v11, v255

.LBB0_37:
	s_or_b64 exec, exec, s[10:11]
	v_readfirstlane_b32 s83, v10
	s_cmp_gt_i32 s83, 0x199ff
	s_mov_b64 s[10:11], -1
	s_cbranch_scc1 .LBB0_32
	s_and_saveexec_b64 s[12:13], s[4:5]
	v_mov_b32_e32 v255, 4
	global_atomic_add v255, v3, v255, s[6:7] sc0
	s_or_b64 exec, exec, s[12:13]
	s_load_dwordx2 s[10:11], s[28:29], 0x40
	s_lshl_b32 s8, s83, 1
	s_lshl_b32 s84, s83, 2
	s_lshl_b32 s85, s83, 6
	s_add_i32 s86, s8, 0xffff7300
	s_add_i32 s87, s83, 4
	s_branch .LBB0_40
